# speedup vs baseline: 1.0544x; 1.0007x over previous
_Z7fc_gemmPKcS0_PKfS2_Pf:
	s_cmpk_gt_u32 s2, 0xff
	s_cbranch_scc1 .Lfc_exit
	s_load_dwordx8 s[4:11], s[0:1], 0x0
	s_load_dwordx2 s[12:13], s[0:1], 0x20
	v_lshrrev_b32_e32 v1, 6, v0
	s_and_b32 s15, s2, 7
	s_lshr_b32 s16, s2, 3
	v_readfirstlane_b32 s14, v1
	v_and_b32_e32 v1, 63, v0
	v_and_b32_e32 v2, 31, v0
	v_bfe_u32 v3, v0, 5, 1
	v_lshrrev_b32_e32 v7, 1, v2
	v_and_b32_e32 v56, 1, v2
	v_lshlrev_b32_e32 v56, 3, v56
	v_xor_b32_e32 v56, v56, v3
	v_xor_b32_e32 v56, v56, v7
	v_lshlrev_b32_e32 v56, 4, v56
	v_lshl_or_b32 v56, v7, 8, v56
	s_lshr_b32 s17, s14, 1
	s_and_b32 s18, s14, 1
	s_lshl_b32 s19, s17, 13
	s_lshl_b32 s27, s18, 13
	s_add_u32 s27, s27, 0x8000
	v_add_u32_e32 v8, s19, v56
	v_add_u32_e32 v12, s27, v56
	v_xor_b32_e32 v9, 32, v8
	v_xor_b32_e32 v13, 32, v12
	v_xor_b32_e32 v10, 64, v8
	v_xor_b32_e32 v14, 64, v12
	v_xor_b32_e32 v11, 96, v8
	v_xor_b32_e32 v15, 96, v12
	v_add_u32_e32 v16, 0x10000, v8
	v_add_u32_e32 v17, 0x10000, v9
	v_add_u32_e32 v18, 0x10000, v10
	v_add_u32_e32 v19, 0x10000, v11
	v_add_u32_e32 v20, 0x10000, v12
	v_add_u32_e32 v21, 0x10000, v13
	v_add_u32_e32 v22, 0x10000, v14
	v_add_u32_e32 v23, 0x10000, v15
	v_lshrrev_b32_e32 v4, 6, v0
	v_lshlrev_b32_e32 v4, 11, v4
	v_lshl_or_b32 v4, v1, 4, v4
	s_lshl_b32 s26, s14, 11
	v_lshlrev_b32_e32 v5, 16, v3
	v_lshl_or_b32 v5, v2, 2, v5
	v_lshlrev_b32_e32 v6, 2, v2
	s_waitcnt lgkmcnt(0)
	s_lshl_b32 s3, s15, 18
	s_add_u32 s20, s4, s3
	s_addc_u32 s21, s5, 0
	s_add_u32 s22, s20, 0x20000
	s_addc_u32 s23, s21, 0
	s_lshl_b32 s3, s16, 17
	s_add_u32 s24, s6, s3
	s_addc_u32 s25, s7, 0
	s_lshl_b32 s3, s16, 9
	s_lshl_b32 s38, s18, 8
	s_add_u32 s3, s3, s38
	s_add_u32 s36, s8, s3
	s_addc_u32 s37, s9, 0
	s_lshl_b32 s38, s15, 22
	s_lshl_b32 s39, s17, 20
	s_add_u32 s38, s38, s39
	s_add_u32 s38, s38, s3
	s_add_u32 s28, s10, s38
	s_addc_u32 s29, s11, 0
	s_add_u32 s30, s12, s38
	s_addc_u32 s31, s13, 0
	global_load_dword v62, v6, s[36:37]
	global_load_dword v63, v6, s[36:37] offset:128
	s_add_u32 m0, s26, 0
	s_nop 0
	global_load_lds_dwordx4 v4, s[20:21]
	global_load_lds_dwordx4 v4, s[20:21] offset:1024
	s_add_u32 m0, s26, 16384
	s_nop 0
	global_load_lds_dwordx4 v4, s[22:23]
	global_load_lds_dwordx4 v4, s[22:23] offset:1024
	s_add_u32 m0, s26, 32768
	s_nop 0
	global_load_lds_dwordx4 v4, s[24:25]
	global_load_lds_dwordx4 v4, s[24:25] offset:1024
	v_add_u32_e32 v4, 0x4000, v4
	s_add_u32 m0, s26, 49152
	s_nop 0
	global_load_lds_dwordx4 v4, s[20:21]
	global_load_lds_dwordx4 v4, s[20:21] offset:1024
	s_add_u32 m0, s26, 65536
	s_nop 0
	global_load_lds_dwordx4 v4, s[22:23]
	global_load_lds_dwordx4 v4, s[22:23] offset:1024
	s_add_u32 m0, s26, 81920
	s_nop 0
	global_load_lds_dwordx4 v4, s[24:25]
	global_load_lds_dwordx4 v4, s[24:25] offset:1024
	v_add_u32_e32 v4, 0x4000, v4
	s_waitcnt vmcnt(6)
	s_barrier
	s_add_u32 m0, s26, 98304
	s_nop 0
	global_load_lds_dwordx4 v4, s[20:21]
	global_load_lds_dwordx4 v4, s[20:21] offset:1024
	s_add_u32 m0, s26, 114688
	s_nop 0
	global_load_lds_dwordx4 v4, s[22:23]
	global_load_lds_dwordx4 v4, s[22:23] offset:1024
	s_add_u32 m0, s26, 131072
	s_nop 0
	global_load_lds_dwordx4 v4, s[24:25]
	global_load_lds_dwordx4 v4, s[24:25] offset:1024
	v_add_u32_e32 v4, 0x4000, v4
	s_add_u32 s32, s28, 0
	s_addc_u32 s33, s29, 0
	global_load_dword v128, v5, s[32:33] nt
	global_load_dword v144, v5, s[32:33] offset:128 nt
	s_add_u32 s34, s28, 16384
	s_addc_u32 s35, s29, 0
	global_load_dword v129, v5, s[34:35] nt
	global_load_dword v145, v5, s[34:35] offset:128 nt
	s_add_u32 s32, s28, 32768
	s_addc_u32 s33, s29, 0
	global_load_dword v130, v5, s[32:33] nt
	global_load_dword v146, v5, s[32:33] offset:128 nt
	s_add_u32 s34, s28, 49152
	s_addc_u32 s35, s29, 0
	global_load_dword v131, v5, s[34:35] nt
	global_load_dword v147, v5, s[34:35] offset:128 nt
	s_add_u32 s32, s28, 131072
	s_addc_u32 s33, s29, 0
	global_load_dword v132, v5, s[32:33] nt
	global_load_dword v148, v5, s[32:33] offset:128 nt
	s_add_u32 s34, s28, 147456
	s_addc_u32 s35, s29, 0
	global_load_dword v133, v5, s[34:35] nt
	global_load_dword v149, v5, s[34:35] offset:128 nt
	s_add_u32 s32, s28, 163840
	s_addc_u32 s33, s29, 0
	global_load_dword v134, v5, s[32:33] nt
	global_load_dword v150, v5, s[32:33] offset:128 nt
	s_add_u32 s34, s28, 180224
	s_addc_u32 s35, s29, 0
	global_load_dword v135, v5, s[34:35] nt
	global_load_dword v151, v5, s[34:35] offset:128 nt
	s_add_u32 s32, s28, 262144
	s_addc_u32 s33, s29, 0
	global_load_dword v136, v5, s[32:33] nt
	global_load_dword v152, v5, s[32:33] offset:128 nt
	s_add_u32 s34, s28, 278528
	s_addc_u32 s35, s29, 0
	global_load_dword v137, v5, s[34:35] nt
	global_load_dword v153, v5, s[34:35] offset:128 nt
	s_add_u32 s32, s28, 294912
	s_addc_u32 s33, s29, 0
	global_load_dword v138, v5, s[32:33] nt
	global_load_dword v154, v5, s[32:33] offset:128 nt
	s_add_u32 s34, s28, 311296
	s_addc_u32 s35, s29, 0
	global_load_dword v139, v5, s[34:35] nt
	global_load_dword v155, v5, s[34:35] offset:128 nt
	s_add_u32 s32, s28, 393216
	s_addc_u32 s33, s29, 0
	global_load_dword v140, v5, s[32:33] nt
	global_load_dword v156, v5, s[32:33] offset:128 nt
	s_add_u32 s34, s28, 409600
	s_addc_u32 s35, s29, 0
	global_load_dword v141, v5, s[34:35] nt
	global_load_dword v157, v5, s[34:35] offset:128 nt
	s_add_u32 s32, s28, 425984
	s_addc_u32 s33, s29, 0
	global_load_dword v142, v5, s[32:33] nt
	global_load_dword v158, v5, s[32:33] offset:128 nt
	s_add_u32 s34, s28, 442368
	s_addc_u32 s35, s29, 0
	global_load_dword v143, v5, s[34:35] nt
	global_load_dword v159, v5, s[34:35] offset:128 nt
	ds_read_b128 v[24:27], v8
	ds_read_b128 v[32:35], v12
	ds_read_b128 v[28:31], v8 offset:4096
	ds_read_b128 v[36:39], v12 offset:4096
	ds_read_b128 v[40:43], v9
	ds_read_b128 v[48:51], v13
	ds_read_b128 v[44:47], v9 offset:4096
	ds_read_b128 v[52:55], v13 offset:4096
	s_waitcnt lgkmcnt(4)
	v_mfma_f32_32x32x16_bf16 v[64:79], v[24:27], v[32:35], 0
	v_mfma_f32_32x32x16_bf16 v[80:95], v[24:27], v[36:39], 0
	v_mfma_f32_32x32x16_bf16 v[96:111], v[28:31], v[32:35], 0
	v_mfma_f32_32x32x16_bf16 v[112:127], v[28:31], v[36:39], 0
	ds_read_b128 v[24:27], v10
	ds_read_b128 v[32:35], v14
	ds_read_b128 v[28:31], v10 offset:4096
	ds_read_b128 v[36:39], v14 offset:4096
	s_waitcnt lgkmcnt(4)
	v_mfma_f32_32x32x16_bf16 v[64:79], v[40:43], v[48:51], v[64:79]
	v_mfma_f32_32x32x16_bf16 v[80:95], v[40:43], v[52:55], v[80:95]
	v_mfma_f32_32x32x16_bf16 v[96:111], v[44:47], v[48:51], v[96:111]
	v_mfma_f32_32x32x16_bf16 v[112:127], v[44:47], v[52:55], v[112:127]
	ds_read_b128 v[40:43], v11
	ds_read_b128 v[48:51], v15
	ds_read_b128 v[44:47], v11 offset:4096
	ds_read_b128 v[52:55], v15 offset:4096
	s_waitcnt lgkmcnt(4)
	v_mfma_f32_32x32x16_bf16 v[64:79], v[24:27], v[32:35], v[64:79]
	v_mfma_f32_32x32x16_bf16 v[80:95], v[24:27], v[36:39], v[80:95]
	v_mfma_f32_32x32x16_bf16 v[96:111], v[28:31], v[32:35], v[96:111]
	v_mfma_f32_32x32x16_bf16 v[112:127], v[28:31], v[36:39], v[112:127]
	s_waitcnt lgkmcnt(0)
	v_mfma_f32_32x32x16_bf16 v[64:79], v[40:43], v[48:51], v[64:79]
	v_mfma_f32_32x32x16_bf16 v[80:95], v[40:43], v[52:55], v[80:95]
	v_mfma_f32_32x32x16_bf16 v[96:111], v[44:47], v[48:51], v[96:111]
	v_mfma_f32_32x32x16_bf16 v[112:127], v[44:47], v[52:55], v[112:127]
	s_waitcnt vmcnt(38)
	s_barrier
	s_add_u32 m0, s26, 0
	s_nop 0
	global_load_lds_dwordx4 v4, s[20:21]
	global_load_lds_dwordx4 v4, s[20:21] offset:1024
	s_add_u32 m0, s26, 16384
	s_nop 0
	global_load_lds_dwordx4 v4, s[22:23]
	global_load_lds_dwordx4 v4, s[22:23] offset:1024
	s_add_u32 m0, s26, 32768
	s_nop 0
	global_load_lds_dwordx4 v4, s[24:25]
	global_load_lds_dwordx4 v4, s[24:25] offset:1024
	v_add_u32_e32 v4, 0x4000, v4
	ds_read_b128 v[24:27], v8 offset:49152
	ds_read_b128 v[32:35], v12 offset:49152
	ds_read_b128 v[28:31], v8 offset:53248
	ds_read_b128 v[36:39], v12 offset:53248
	ds_read_b128 v[40:43], v9 offset:49152
	ds_read_b128 v[48:51], v13 offset:49152
	ds_read_b128 v[44:47], v9 offset:53248
	ds_read_b128 v[52:55], v13 offset:53248
	s_waitcnt lgkmcnt(4)
	v_mfma_f32_32x32x16_bf16 v[64:79], v[24:27], v[32:35], v[64:79]
	v_mfma_f32_32x32x16_bf16 v[80:95], v[24:27], v[36:39], v[80:95]
	v_mfma_f32_32x32x16_bf16 v[96:111], v[28:31], v[32:35], v[96:111]
	v_mfma_f32_32x32x16_bf16 v[112:127], v[28:31], v[36:39], v[112:127]
	ds_read_b128 v[24:27], v10 offset:49152
	ds_read_b128 v[32:35], v14 offset:49152
	ds_read_b128 v[28:31], v10 offset:53248
	ds_read_b128 v[36:39], v14 offset:53248
	s_waitcnt lgkmcnt(4)
	v_mfma_f32_32x32x16_bf16 v[64:79], v[40:43], v[48:51], v[64:79]
	v_mfma_f32_32x32x16_bf16 v[80:95], v[40:43], v[52:55], v[80:95]
	v_mfma_f32_32x32x16_bf16 v[96:111], v[44:47], v[48:51], v[96:111]
	v_mfma_f32_32x32x16_bf16 v[112:127], v[44:47], v[52:55], v[112:127]
	ds_read_b128 v[40:43], v11 offset:49152
	ds_read_b128 v[48:51], v15 offset:49152
	ds_read_b128 v[44:47], v11 offset:53248
	ds_read_b128 v[52:55], v15 offset:53248
	s_waitcnt lgkmcnt(4)
	v_mfma_f32_32x32x16_bf16 v[64:79], v[24:27], v[32:35], v[64:79]
	v_mfma_f32_32x32x16_bf16 v[80:95], v[24:27], v[36:39], v[80:95]
	v_mfma_f32_32x32x16_bf16 v[96:111], v[28:31], v[32:35], v[96:111]
	v_mfma_f32_32x32x16_bf16 v[112:127], v[28:31], v[36:39], v[112:127]
	s_waitcnt lgkmcnt(0)
	v_mfma_f32_32x32x16_bf16 v[64:79], v[40:43], v[48:51], v[64:79]
	v_mfma_f32_32x32x16_bf16 v[80:95], v[40:43], v[52:55], v[80:95]
	v_mfma_f32_32x32x16_bf16 v[96:111], v[44:47], v[48:51], v[96:111]
	v_mfma_f32_32x32x16_bf16 v[112:127], v[44:47], v[52:55], v[112:127]
	s_waitcnt vmcnt(38)
	s_barrier
	s_add_u32 m0, s26, 49152
	s_nop 0
	global_load_lds_dwordx4 v4, s[20:21]
	global_load_lds_dwordx4 v4, s[20:21] offset:1024
	s_add_u32 m0, s26, 65536
	s_nop 0
	global_load_lds_dwordx4 v4, s[22:23]
	global_load_lds_dwordx4 v4, s[22:23] offset:1024
	s_add_u32 m0, s26, 81920
	s_nop 0
	global_load_lds_dwordx4 v4, s[24:25]
	global_load_lds_dwordx4 v4, s[24:25] offset:1024
	v_add_u32_e32 v4, 0x4000, v4
	ds_read_b128 v[24:27], v16 offset:32768
	ds_read_b128 v[32:35], v20 offset:32768
	ds_read_b128 v[28:31], v16 offset:36864
	ds_read_b128 v[36:39], v20 offset:36864
	ds_read_b128 v[40:43], v17 offset:32768
	ds_read_b128 v[48:51], v21 offset:32768
	ds_read_b128 v[44:47], v17 offset:36864
	ds_read_b128 v[52:55], v21 offset:36864
	s_waitcnt lgkmcnt(4)
	v_mfma_f32_32x32x16_bf16 v[64:79], v[24:27], v[32:35], v[64:79]
	v_mfma_f32_32x32x16_bf16 v[80:95], v[24:27], v[36:39], v[80:95]
	v_mfma_f32_32x32x16_bf16 v[96:111], v[28:31], v[32:35], v[96:111]
	v_mfma_f32_32x32x16_bf16 v[112:127], v[28:31], v[36:39], v[112:127]
	ds_read_b128 v[24:27], v18 offset:32768
	ds_read_b128 v[32:35], v22 offset:32768
	ds_read_b128 v[28:31], v18 offset:36864
	ds_read_b128 v[36:39], v22 offset:36864
	s_waitcnt lgkmcnt(4)
	v_mfma_f32_32x32x16_bf16 v[64:79], v[40:43], v[48:51], v[64:79]
	v_mfma_f32_32x32x16_bf16 v[80:95], v[40:43], v[52:55], v[80:95]
	v_mfma_f32_32x32x16_bf16 v[96:111], v[44:47], v[48:51], v[96:111]
	v_mfma_f32_32x32x16_bf16 v[112:127], v[44:47], v[52:55], v[112:127]
	ds_read_b128 v[40:43], v19 offset:32768
	ds_read_b128 v[48:51], v23 offset:32768
	ds_read_b128 v[44:47], v19 offset:36864
	ds_read_b128 v[52:55], v23 offset:36864
	s_waitcnt lgkmcnt(4)
	v_mfma_f32_32x32x16_bf16 v[64:79], v[24:27], v[32:35], v[64:79]
	v_mfma_f32_32x32x16_bf16 v[80:95], v[24:27], v[36:39], v[80:95]
	v_mfma_f32_32x32x16_bf16 v[96:111], v[28:31], v[32:35], v[96:111]
	v_mfma_f32_32x32x16_bf16 v[112:127], v[28:31], v[36:39], v[112:127]
	s_waitcnt lgkmcnt(0)
	v_mfma_f32_32x32x16_bf16 v[64:79], v[40:43], v[48:51], v[64:79]
	v_mfma_f32_32x32x16_bf16 v[80:95], v[40:43], v[52:55], v[80:95]
	v_mfma_f32_32x32x16_bf16 v[96:111], v[44:47], v[48:51], v[96:111]
	v_mfma_f32_32x32x16_bf16 v[112:127], v[44:47], v[52:55], v[112:127]
	s_waitcnt vmcnt(6)
	s_barrier
	s_add_u32 m0, s26, 98304
	s_nop 0
	global_load_lds_dwordx4 v4, s[20:21]
	global_load_lds_dwordx4 v4, s[20:21] offset:1024
	s_add_u32 m0, s26, 114688
	s_nop 0
	global_load_lds_dwordx4 v4, s[22:23]
	global_load_lds_dwordx4 v4, s[22:23] offset:1024
	s_add_u32 m0, s26, 131072
	s_nop 0
	global_load_lds_dwordx4 v4, s[24:25]
	global_load_lds_dwordx4 v4, s[24:25] offset:1024
	v_add_u32_e32 v4, 0x4000, v4
	s_add_u32 s32, s28, 524288
	s_addc_u32 s33, s29, 0
	global_load_dword v160, v5, s[32:33] nt
	global_load_dword v176, v5, s[32:33] offset:128 nt
	s_add_u32 s34, s28, 540672
	s_addc_u32 s35, s29, 0
	global_load_dword v161, v5, s[34:35] nt
	global_load_dword v177, v5, s[34:35] offset:128 nt
	s_add_u32 s32, s28, 557056
	s_addc_u32 s33, s29, 0
	global_load_dword v162, v5, s[32:33] nt
	global_load_dword v178, v5, s[32:33] offset:128 nt
	s_add_u32 s34, s28, 573440
	s_addc_u32 s35, s29, 0
	global_load_dword v163, v5, s[34:35] nt
	global_load_dword v179, v5, s[34:35] offset:128 nt
	s_add_u32 s32, s28, 655360
	s_addc_u32 s33, s29, 0
	global_load_dword v164, v5, s[32:33] nt
	global_load_dword v180, v5, s[32:33] offset:128 nt
	s_add_u32 s34, s28, 671744
	s_addc_u32 s35, s29, 0
	global_load_dword v165, v5, s[34:35] nt
	global_load_dword v181, v5, s[34:35] offset:128 nt
	s_add_u32 s32, s28, 688128
	s_addc_u32 s33, s29, 0
	global_load_dword v166, v5, s[32:33] nt
	global_load_dword v182, v5, s[32:33] offset:128 nt
	s_add_u32 s34, s28, 704512
	s_addc_u32 s35, s29, 0
	global_load_dword v167, v5, s[34:35] nt
	global_load_dword v183, v5, s[34:35] offset:128 nt
	s_add_u32 s32, s28, 786432
	s_addc_u32 s33, s29, 0
	global_load_dword v168, v5, s[32:33] nt
	global_load_dword v184, v5, s[32:33] offset:128 nt
	s_add_u32 s34, s28, 802816
	s_addc_u32 s35, s29, 0
	global_load_dword v169, v5, s[34:35] nt
	global_load_dword v185, v5, s[34:35] offset:128 nt
	s_add_u32 s32, s28, 819200
	s_addc_u32 s33, s29, 0
	global_load_dword v170, v5, s[32:33] nt
	global_load_dword v186, v5, s[32:33] offset:128 nt
	s_add_u32 s34, s28, 835584
	s_addc_u32 s35, s29, 0
	global_load_dword v171, v5, s[34:35] nt
	global_load_dword v187, v5, s[34:35] offset:128 nt
	s_add_u32 s32, s28, 917504
	s_addc_u32 s33, s29, 0
	global_load_dword v172, v5, s[32:33] nt
	global_load_dword v188, v5, s[32:33] offset:128 nt
	s_add_u32 s34, s28, 933888
	s_addc_u32 s35, s29, 0
	global_load_dword v173, v5, s[34:35] nt
	global_load_dword v189, v5, s[34:35] offset:128 nt
	s_add_u32 s32, s28, 950272
	s_addc_u32 s33, s29, 0
	global_load_dword v174, v5, s[32:33] nt
	global_load_dword v190, v5, s[32:33] offset:128 nt
	s_add_u32 s34, s28, 966656
	s_addc_u32 s35, s29, 0
	global_load_dword v175, v5, s[34:35] nt
	global_load_dword v191, v5, s[34:35] offset:128 nt
	ds_read_b128 v[24:27], v8
	ds_read_b128 v[32:35], v12
	ds_read_b128 v[28:31], v8 offset:4096
	ds_read_b128 v[36:39], v12 offset:4096
	ds_read_b128 v[40:43], v9
	ds_read_b128 v[48:51], v13
	ds_read_b128 v[44:47], v9 offset:4096
	ds_read_b128 v[52:55], v13 offset:4096
	s_waitcnt lgkmcnt(4)
	v_mfma_f32_32x32x16_bf16 v[64:79], v[24:27], v[32:35], v[64:79]
	v_mfma_f32_32x32x16_bf16 v[80:95], v[24:27], v[36:39], v[80:95]
	v_mfma_f32_32x32x16_bf16 v[96:111], v[28:31], v[32:35], v[96:111]
	v_mfma_f32_32x32x16_bf16 v[112:127], v[28:31], v[36:39], v[112:127]
	ds_read_b128 v[24:27], v10
	ds_read_b128 v[32:35], v14
	ds_read_b128 v[28:31], v10 offset:4096
	ds_read_b128 v[36:39], v14 offset:4096
	s_waitcnt lgkmcnt(4)
	v_mfma_f32_32x32x16_bf16 v[64:79], v[40:43], v[48:51], v[64:79]
	v_mfma_f32_32x32x16_bf16 v[80:95], v[40:43], v[52:55], v[80:95]
	v_mfma_f32_32x32x16_bf16 v[96:111], v[44:47], v[48:51], v[96:111]
	v_mfma_f32_32x32x16_bf16 v[112:127], v[44:47], v[52:55], v[112:127]
	ds_read_b128 v[40:43], v11
	ds_read_b128 v[48:51], v15
	ds_read_b128 v[44:47], v11 offset:4096
	ds_read_b128 v[52:55], v15 offset:4096
	s_waitcnt lgkmcnt(4)
	v_mfma_f32_32x32x16_bf16 v[64:79], v[24:27], v[32:35], v[64:79]
	v_mfma_f32_32x32x16_bf16 v[80:95], v[24:27], v[36:39], v[80:95]
	v_mfma_f32_32x32x16_bf16 v[96:111], v[28:31], v[32:35], v[96:111]
	v_mfma_f32_32x32x16_bf16 v[112:127], v[28:31], v[36:39], v[112:127]
	s_waitcnt lgkmcnt(0)
	v_mfma_f32_32x32x16_bf16 v[64:79], v[40:43], v[48:51], v[64:79]
	v_mfma_f32_32x32x16_bf16 v[80:95], v[40:43], v[52:55], v[80:95]
	v_mfma_f32_32x32x16_bf16 v[96:111], v[44:47], v[48:51], v[96:111]
	v_mfma_f32_32x32x16_bf16 v[112:127], v[44:47], v[52:55], v[112:127]
	s_waitcnt vmcnt(38)
	s_barrier
	s_add_u32 m0, s26, 0
	s_nop 0
	global_load_lds_dwordx4 v4, s[20:21]
	global_load_lds_dwordx4 v4, s[20:21] offset:1024
	s_add_u32 m0, s26, 16384
	s_nop 0
	global_load_lds_dwordx4 v4, s[22:23]
	global_load_lds_dwordx4 v4, s[22:23] offset:1024
	s_add_u32 m0, s26, 32768
	s_nop 0
	global_load_lds_dwordx4 v4, s[24:25]
	global_load_lds_dwordx4 v4, s[24:25] offset:1024
	v_add_u32_e32 v4, 0x4000, v4
	ds_read_b128 v[24:27], v8 offset:49152
	ds_read_b128 v[32:35], v12 offset:49152
	ds_read_b128 v[28:31], v8 offset:53248
	ds_read_b128 v[36:39], v12 offset:53248
	ds_read_b128 v[40:43], v9 offset:49152
	ds_read_b128 v[48:51], v13 offset:49152
	ds_read_b128 v[44:47], v9 offset:53248
	ds_read_b128 v[52:55], v13 offset:53248
	s_waitcnt lgkmcnt(4)
	v_mfma_f32_32x32x16_bf16 v[64:79], v[24:27], v[32:35], v[64:79]
	v_mfma_f32_32x32x16_bf16 v[80:95], v[24:27], v[36:39], v[80:95]
	v_mfma_f32_32x32x16_bf16 v[96:111], v[28:31], v[32:35], v[96:111]
	v_mfma_f32_32x32x16_bf16 v[112:127], v[28:31], v[36:39], v[112:127]
	ds_read_b128 v[24:27], v10 offset:49152
	ds_read_b128 v[32:35], v14 offset:49152
	ds_read_b128 v[28:31], v10 offset:53248
	ds_read_b128 v[36:39], v14 offset:53248
	s_waitcnt lgkmcnt(4)
	v_mfma_f32_32x32x16_bf16 v[64:79], v[40:43], v[48:51], v[64:79]
	v_mfma_f32_32x32x16_bf16 v[80:95], v[40:43], v[52:55], v[80:95]
	v_mfma_f32_32x32x16_bf16 v[96:111], v[44:47], v[48:51], v[96:111]
	v_mfma_f32_32x32x16_bf16 v[112:127], v[44:47], v[52:55], v[112:127]
	ds_read_b128 v[40:43], v11 offset:49152
	ds_read_b128 v[48:51], v15 offset:49152
	ds_read_b128 v[44:47], v11 offset:53248
	ds_read_b128 v[52:55], v15 offset:53248
	s_waitcnt lgkmcnt(4)
	v_mfma_f32_32x32x16_bf16 v[64:79], v[24:27], v[32:35], v[64:79]
	v_mfma_f32_32x32x16_bf16 v[80:95], v[24:27], v[36:39], v[80:95]
	v_mfma_f32_32x32x16_bf16 v[96:111], v[28:31], v[32:35], v[96:111]
	v_mfma_f32_32x32x16_bf16 v[112:127], v[28:31], v[36:39], v[112:127]
	s_waitcnt lgkmcnt(0)
	v_mfma_f32_32x32x16_bf16 v[64:79], v[40:43], v[48:51], v[64:79]
	v_mfma_f32_32x32x16_bf16 v[80:95], v[40:43], v[52:55], v[80:95]
	v_mfma_f32_32x32x16_bf16 v[96:111], v[44:47], v[48:51], v[96:111]
	v_mfma_f32_32x32x16_bf16 v[112:127], v[44:47], v[52:55], v[112:127]
	s_waitcnt vmcnt(38)
	s_barrier
	s_add_u32 m0, s26, 49152
	s_nop 0
	global_load_lds_dwordx4 v4, s[20:21]
	global_load_lds_dwordx4 v4, s[20:21] offset:1024
	s_add_u32 m0, s26, 65536
	s_nop 0
	global_load_lds_dwordx4 v4, s[22:23]
	global_load_lds_dwordx4 v4, s[22:23] offset:1024
	s_add_u32 m0, s26, 81920
	s_nop 0
	global_load_lds_dwordx4 v4, s[24:25]
	global_load_lds_dwordx4 v4, s[24:25] offset:1024
	v_add_u32_e32 v4, 0x4000, v4
	ds_read_b128 v[24:27], v16 offset:32768
	ds_read_b128 v[32:35], v20 offset:32768
	ds_read_b128 v[28:31], v16 offset:36864
	ds_read_b128 v[36:39], v20 offset:36864
	ds_read_b128 v[40:43], v17 offset:32768
	ds_read_b128 v[48:51], v21 offset:32768
	ds_read_b128 v[44:47], v17 offset:36864
	ds_read_b128 v[52:55], v21 offset:36864
	s_waitcnt lgkmcnt(4)
	v_mfma_f32_32x32x16_bf16 v[64:79], v[24:27], v[32:35], v[64:79]
	v_mfma_f32_32x32x16_bf16 v[80:95], v[24:27], v[36:39], v[80:95]
	v_mfma_f32_32x32x16_bf16 v[96:111], v[28:31], v[32:35], v[96:111]
	v_mfma_f32_32x32x16_bf16 v[112:127], v[28:31], v[36:39], v[112:127]
	ds_read_b128 v[24:27], v18 offset:32768
	ds_read_b128 v[32:35], v22 offset:32768
	ds_read_b128 v[28:31], v18 offset:36864
	ds_read_b128 v[36:39], v22 offset:36864
	s_waitcnt lgkmcnt(4)
	v_mfma_f32_32x32x16_bf16 v[64:79], v[40:43], v[48:51], v[64:79]
	v_mfma_f32_32x32x16_bf16 v[80:95], v[40:43], v[52:55], v[80:95]
	v_mfma_f32_32x32x16_bf16 v[96:111], v[44:47], v[48:51], v[96:111]
	v_mfma_f32_32x32x16_bf16 v[112:127], v[44:47], v[52:55], v[112:127]
	ds_read_b128 v[40:43], v19 offset:32768
	ds_read_b128 v[48:51], v23 offset:32768
	ds_read_b128 v[44:47], v19 offset:36864
	ds_read_b128 v[52:55], v23 offset:36864
	s_waitcnt lgkmcnt(4)
	v_mfma_f32_32x32x16_bf16 v[64:79], v[24:27], v[32:35], v[64:79]
	v_mfma_f32_32x32x16_bf16 v[80:95], v[24:27], v[36:39], v[80:95]
	v_mfma_f32_32x32x16_bf16 v[96:111], v[28:31], v[32:35], v[96:111]
	v_mfma_f32_32x32x16_bf16 v[112:127], v[28:31], v[36:39], v[112:127]
	s_waitcnt lgkmcnt(0)
	v_mfma_f32_32x32x16_bf16 v[64:79], v[40:43], v[48:51], v[64:79]
	v_mfma_f32_32x32x16_bf16 v[80:95], v[40:43], v[52:55], v[80:95]
	v_mfma_f32_32x32x16_bf16 v[96:111], v[44:47], v[48:51], v[96:111]
	v_mfma_f32_32x32x16_bf16 v[112:127], v[44:47], v[52:55], v[112:127]
	s_waitcnt vmcnt(6)
	s_barrier
	ds_read_b128 v[24:27], v8
	ds_read_b128 v[32:35], v12
	ds_read_b128 v[28:31], v8 offset:4096
	ds_read_b128 v[36:39], v12 offset:4096
	ds_read_b128 v[40:43], v9
	ds_read_b128 v[48:51], v13
	ds_read_b128 v[44:47], v9 offset:4096
	ds_read_b128 v[52:55], v13 offset:4096
	s_waitcnt lgkmcnt(4)
	v_mfma_f32_32x32x16_bf16 v[64:79], v[24:27], v[32:35], v[64:79]
	v_mfma_f32_32x32x16_bf16 v[80:95], v[24:27], v[36:39], v[80:95]
	v_mfma_f32_32x32x16_bf16 v[96:111], v[28:31], v[32:35], v[96:111]
	v_mfma_f32_32x32x16_bf16 v[112:127], v[28:31], v[36:39], v[112:127]
	ds_read_b128 v[24:27], v10
	ds_read_b128 v[32:35], v14
	ds_read_b128 v[28:31], v10 offset:4096
	ds_read_b128 v[36:39], v14 offset:4096
	s_waitcnt lgkmcnt(4)
	v_mfma_f32_32x32x16_bf16 v[64:79], v[40:43], v[48:51], v[64:79]
	v_mfma_f32_32x32x16_bf16 v[80:95], v[40:43], v[52:55], v[80:95]
	v_mfma_f32_32x32x16_bf16 v[96:111], v[44:47], v[48:51], v[96:111]
	v_mfma_f32_32x32x16_bf16 v[112:127], v[44:47], v[52:55], v[112:127]
	ds_read_b128 v[40:43], v11
	ds_read_b128 v[48:51], v15
	ds_read_b128 v[44:47], v11 offset:4096
	ds_read_b128 v[52:55], v15 offset:4096
	s_waitcnt lgkmcnt(4)
	v_mfma_f32_32x32x16_bf16 v[64:79], v[24:27], v[32:35], v[64:79]
	v_mfma_f32_32x32x16_bf16 v[80:95], v[24:27], v[36:39], v[80:95]
	v_mfma_f32_32x32x16_bf16 v[96:111], v[28:31], v[32:35], v[96:111]
	v_mfma_f32_32x32x16_bf16 v[112:127], v[28:31], v[36:39], v[112:127]
	s_waitcnt lgkmcnt(0)
	v_mfma_f32_32x32x16_bf16 v[64:79], v[40:43], v[48:51], v[64:79]
	v_mfma_f32_32x32x16_bf16 v[80:95], v[40:43], v[52:55], v[80:95]
	v_mfma_f32_32x32x16_bf16 v[96:111], v[44:47], v[48:51], v[96:111]
	v_mfma_f32_32x32x16_bf16 v[112:127], v[44:47], v[52:55], v[112:127]
	s_waitcnt vmcnt(0)
	s_barrier
	ds_read_b128 v[24:27], v8 offset:49152
	ds_read_b128 v[32:35], v12 offset:49152
	ds_read_b128 v[28:31], v8 offset:53248
	ds_read_b128 v[36:39], v12 offset:53248
	ds_read_b128 v[40:43], v9 offset:49152
	ds_read_b128 v[48:51], v13 offset:49152
	ds_read_b128 v[44:47], v9 offset:53248
	ds_read_b128 v[52:55], v13 offset:53248
	s_waitcnt lgkmcnt(4)
	v_mfma_f32_32x32x16_bf16 v[64:79], v[24:27], v[32:35], v[64:79]
	v_mfma_f32_32x32x16_bf16 v[80:95], v[24:27], v[36:39], v[80:95]
	v_mfma_f32_32x32x16_bf16 v[96:111], v[28:31], v[32:35], v[96:111]
	v_mfma_f32_32x32x16_bf16 v[112:127], v[28:31], v[36:39], v[112:127]
	ds_read_b128 v[24:27], v10 offset:49152
	ds_read_b128 v[32:35], v14 offset:49152
	ds_read_b128 v[28:31], v10 offset:53248
	ds_read_b128 v[36:39], v14 offset:53248
	s_waitcnt lgkmcnt(4)
	v_mfma_f32_32x32x16_bf16 v[64:79], v[40:43], v[48:51], v[64:79]
	v_mfma_f32_32x32x16_bf16 v[80:95], v[40:43], v[52:55], v[80:95]
	v_mfma_f32_32x32x16_bf16 v[96:111], v[44:47], v[48:51], v[96:111]
	v_mfma_f32_32x32x16_bf16 v[112:127], v[44:47], v[52:55], v[112:127]
	ds_read_b128 v[40:43], v11 offset:49152
	ds_read_b128 v[48:51], v15 offset:49152
	ds_read_b128 v[44:47], v11 offset:53248
	ds_read_b128 v[52:55], v15 offset:53248
	s_waitcnt lgkmcnt(4)
	v_mfma_f32_32x32x16_bf16 v[64:79], v[24:27], v[32:35], v[64:79]
	v_mfma_f32_32x32x16_bf16 v[80:95], v[24:27], v[36:39], v[80:95]
	v_mfma_f32_32x32x16_bf16 v[96:111], v[28:31], v[32:35], v[96:111]
	v_mfma_f32_32x32x16_bf16 v[112:127], v[28:31], v[36:39], v[112:127]
	s_waitcnt lgkmcnt(0)
	v_mfma_f32_32x32x16_bf16 v[64:79], v[40:43], v[48:51], v[64:79]
	v_mfma_f32_32x32x16_bf16 v[80:95], v[40:43], v[52:55], v[80:95]
	v_mfma_f32_32x32x16_bf16 v[96:111], v[44:47], v[48:51], v[96:111]
	v_mfma_f32_32x32x16_bf16 v[112:127], v[44:47], v[52:55], v[112:127]
	s_nop 15
	s_nop 3
	s_add_u32 s32, s30, 0
	s_addc_u32 s33, s31, 0
	v_add_f32_e32 v64, v64, v62
	v_add_f32_e32 v64, v64, v128
	v_add_f32_e32 v80, v80, v63
	v_add_f32_e32 v80, v80, v144
	global_store_dword v5, v64, s[32:33] sc1
	global_store_dword v5, v80, s[32:33] offset:128 sc1
	s_add_u32 s34, s30, 16384
	s_addc_u32 s35, s31, 0
	v_add_f32_e32 v65, v65, v62
	v_add_f32_e32 v65, v65, v129
	v_add_f32_e32 v81, v81, v63
	v_add_f32_e32 v81, v81, v145
	global_store_dword v5, v65, s[34:35] sc1
	global_store_dword v5, v81, s[34:35] offset:128 sc1
	s_add_u32 s32, s30, 32768
	s_addc_u32 s33, s31, 0
	v_add_f32_e32 v66, v66, v62
	v_add_f32_e32 v66, v66, v130
	v_add_f32_e32 v82, v82, v63
	v_add_f32_e32 v82, v82, v146
	global_store_dword v5, v66, s[32:33] sc1
	global_store_dword v5, v82, s[32:33] offset:128 sc1
	s_add_u32 s34, s30, 49152
	s_addc_u32 s35, s31, 0
	v_add_f32_e32 v67, v67, v62
	v_add_f32_e32 v67, v67, v131
	v_add_f32_e32 v83, v83, v63
	v_add_f32_e32 v83, v83, v147
	global_store_dword v5, v67, s[34:35] sc1
	global_store_dword v5, v83, s[34:35] offset:128 sc1
	s_add_u32 s32, s30, 131072
	s_addc_u32 s33, s31, 0
	v_add_f32_e32 v68, v68, v62
	v_add_f32_e32 v68, v68, v132
	v_add_f32_e32 v84, v84, v63
	v_add_f32_e32 v84, v84, v148
	global_store_dword v5, v68, s[32:33] sc1
	global_store_dword v5, v84, s[32:33] offset:128 sc1
	s_add_u32 s34, s30, 147456
	s_addc_u32 s35, s31, 0
	v_add_f32_e32 v69, v69, v62
	v_add_f32_e32 v69, v69, v133
	v_add_f32_e32 v85, v85, v63
	v_add_f32_e32 v85, v85, v149
	global_store_dword v5, v69, s[34:35] sc1
	global_store_dword v5, v85, s[34:35] offset:128 sc1
	s_add_u32 s32, s30, 163840
	s_addc_u32 s33, s31, 0
	v_add_f32_e32 v70, v70, v62
	v_add_f32_e32 v70, v70, v134
	v_add_f32_e32 v86, v86, v63
	v_add_f32_e32 v86, v86, v150
	global_store_dword v5, v70, s[32:33] sc1
	global_store_dword v5, v86, s[32:33] offset:128 sc1
	s_add_u32 s34, s30, 180224
	s_addc_u32 s35, s31, 0
	v_add_f32_e32 v71, v71, v62
	v_add_f32_e32 v71, v71, v135
	v_add_f32_e32 v87, v87, v63
	v_add_f32_e32 v87, v87, v151
	global_store_dword v5, v71, s[34:35] sc1
	global_store_dword v5, v87, s[34:35] offset:128 sc1
	s_add_u32 s32, s30, 262144
	s_addc_u32 s33, s31, 0
	v_add_f32_e32 v72, v72, v62
	v_add_f32_e32 v72, v72, v136
	v_add_f32_e32 v88, v88, v63
	v_add_f32_e32 v88, v88, v152
	global_store_dword v5, v72, s[32:33] sc1
	global_store_dword v5, v88, s[32:33] offset:128 sc1
	s_add_u32 s34, s30, 278528
	s_addc_u32 s35, s31, 0
	v_add_f32_e32 v73, v73, v62
	v_add_f32_e32 v73, v73, v137
	v_add_f32_e32 v89, v89, v63
	v_add_f32_e32 v89, v89, v153
	global_store_dword v5, v73, s[34:35] sc1
	global_store_dword v5, v89, s[34:35] offset:128 sc1
	s_add_u32 s32, s30, 294912
	s_addc_u32 s33, s31, 0
	v_add_f32_e32 v74, v74, v62
	v_add_f32_e32 v74, v74, v138
	v_add_f32_e32 v90, v90, v63
	v_add_f32_e32 v90, v90, v154
	global_store_dword v5, v74, s[32:33] sc1
	global_store_dword v5, v90, s[32:33] offset:128 sc1
	s_add_u32 s34, s30, 311296
	s_addc_u32 s35, s31, 0
	v_add_f32_e32 v75, v75, v62
	v_add_f32_e32 v75, v75, v139
	v_add_f32_e32 v91, v91, v63
	v_add_f32_e32 v91, v91, v155
	global_store_dword v5, v75, s[34:35] sc1
	global_store_dword v5, v91, s[34:35] offset:128 sc1
	s_add_u32 s32, s30, 393216
	s_addc_u32 s33, s31, 0
	v_add_f32_e32 v76, v76, v62
	v_add_f32_e32 v76, v76, v140
	v_add_f32_e32 v92, v92, v63
	v_add_f32_e32 v92, v92, v156
	global_store_dword v5, v76, s[32:33] sc1
	global_store_dword v5, v92, s[32:33] offset:128 sc1
	s_add_u32 s34, s30, 409600
	s_addc_u32 s35, s31, 0
	v_add_f32_e32 v77, v77, v62
	v_add_f32_e32 v77, v77, v141
	v_add_f32_e32 v93, v93, v63
	v_add_f32_e32 v93, v93, v157
	global_store_dword v5, v77, s[34:35] sc1
	global_store_dword v5, v93, s[34:35] offset:128 sc1
	s_add_u32 s32, s30, 425984
	s_addc_u32 s33, s31, 0
	v_add_f32_e32 v78, v78, v62
	v_add_f32_e32 v78, v78, v142
	v_add_f32_e32 v94, v94, v63
	v_add_f32_e32 v94, v94, v158
	global_store_dword v5, v78, s[32:33] sc1
	global_store_dword v5, v94, s[32:33] offset:128 sc1
	s_add_u32 s34, s30, 442368
	s_addc_u32 s35, s31, 0
	v_add_f32_e32 v79, v79, v62
	v_add_f32_e32 v79, v79, v143
	v_add_f32_e32 v95, v95, v63
	v_add_f32_e32 v95, v95, v159
	global_store_dword v5, v79, s[34:35] sc1
	global_store_dword v5, v95, s[34:35] offset:128 sc1
	s_add_u32 s32, s30, 524288
	s_addc_u32 s33, s31, 0
	v_add_f32_e32 v96, v96, v62
	v_add_f32_e32 v96, v96, v160
	v_add_f32_e32 v112, v112, v63
	v_add_f32_e32 v112, v112, v176
	global_store_dword v5, v96, s[32:33] sc1
	global_store_dword v5, v112, s[32:33] offset:128 sc1
	s_add_u32 s34, s30, 540672
	s_addc_u32 s35, s31, 0
	v_add_f32_e32 v97, v97, v62
	v_add_f32_e32 v97, v97, v161
	v_add_f32_e32 v113, v113, v63
	v_add_f32_e32 v113, v113, v177
	global_store_dword v5, v97, s[34:35] sc1
	global_store_dword v5, v113, s[34:35] offset:128 sc1
	s_add_u32 s32, s30, 557056
	s_addc_u32 s33, s31, 0
	v_add_f32_e32 v98, v98, v62
	v_add_f32_e32 v98, v98, v162
	v_add_f32_e32 v114, v114, v63
	v_add_f32_e32 v114, v114, v178
	global_store_dword v5, v98, s[32:33] sc1
	global_store_dword v5, v114, s[32:33] offset:128 sc1
	s_add_u32 s34, s30, 573440
	s_addc_u32 s35, s31, 0
	v_add_f32_e32 v99, v99, v62
	v_add_f32_e32 v99, v99, v163
	v_add_f32_e32 v115, v115, v63
	v_add_f32_e32 v115, v115, v179
	global_store_dword v5, v99, s[34:35] sc1
	global_store_dword v5, v115, s[34:35] offset:128 sc1
	s_add_u32 s32, s30, 655360
	s_addc_u32 s33, s31, 0
	v_add_f32_e32 v100, v100, v62
	v_add_f32_e32 v100, v100, v164
	v_add_f32_e32 v116, v116, v63
	v_add_f32_e32 v116, v116, v180
	global_store_dword v5, v100, s[32:33] sc1
	global_store_dword v5, v116, s[32:33] offset:128 sc1
	s_add_u32 s34, s30, 671744
	s_addc_u32 s35, s31, 0
	v_add_f32_e32 v101, v101, v62
	v_add_f32_e32 v101, v101, v165
	v_add_f32_e32 v117, v117, v63
	v_add_f32_e32 v117, v117, v181
	global_store_dword v5, v101, s[34:35] sc1
	global_store_dword v5, v117, s[34:35] offset:128 sc1
	s_add_u32 s32, s30, 688128
	s_addc_u32 s33, s31, 0
	v_add_f32_e32 v102, v102, v62
	v_add_f32_e32 v102, v102, v166
	v_add_f32_e32 v118, v118, v63
	v_add_f32_e32 v118, v118, v182
	global_store_dword v5, v102, s[32:33] sc1
	global_store_dword v5, v118, s[32:33] offset:128 sc1
	s_add_u32 s34, s30, 704512
	s_addc_u32 s35, s31, 0
	v_add_f32_e32 v103, v103, v62
	v_add_f32_e32 v103, v103, v167
	v_add_f32_e32 v119, v119, v63
	v_add_f32_e32 v119, v119, v183
	global_store_dword v5, v103, s[34:35] sc1
	global_store_dword v5, v119, s[34:35] offset:128 sc1
	s_add_u32 s32, s30, 786432
	s_addc_u32 s33, s31, 0
	v_add_f32_e32 v104, v104, v62
	v_add_f32_e32 v104, v104, v168
	v_add_f32_e32 v120, v120, v63
	v_add_f32_e32 v120, v120, v184
	global_store_dword v5, v104, s[32:33] sc1
	global_store_dword v5, v120, s[32:33] offset:128 sc1
	s_add_u32 s34, s30, 802816
	s_addc_u32 s35, s31, 0
	v_add_f32_e32 v105, v105, v62
	v_add_f32_e32 v105, v105, v169
	v_add_f32_e32 v121, v121, v63
	v_add_f32_e32 v121, v121, v185
	global_store_dword v5, v105, s[34:35] sc1
	global_store_dword v5, v121, s[34:35] offset:128 sc1
	s_add_u32 s32, s30, 819200
	s_addc_u32 s33, s31, 0
	v_add_f32_e32 v106, v106, v62
	v_add_f32_e32 v106, v106, v170
	v_add_f32_e32 v122, v122, v63
	v_add_f32_e32 v122, v122, v186
	global_store_dword v5, v106, s[32:33] sc1
	global_store_dword v5, v122, s[32:33] offset:128 sc1
	s_add_u32 s34, s30, 835584
	s_addc_u32 s35, s31, 0
	v_add_f32_e32 v107, v107, v62
	v_add_f32_e32 v107, v107, v171
	v_add_f32_e32 v123, v123, v63
	v_add_f32_e32 v123, v123, v187
	global_store_dword v5, v107, s[34:35] sc1
	global_store_dword v5, v123, s[34:35] offset:128 sc1
	s_add_u32 s32, s30, 917504
	s_addc_u32 s33, s31, 0
	v_add_f32_e32 v108, v108, v62
	v_add_f32_e32 v108, v108, v172
	v_add_f32_e32 v124, v124, v63
	v_add_f32_e32 v124, v124, v188
	global_store_dword v5, v108, s[32:33] sc1
	global_store_dword v5, v124, s[32:33] offset:128 sc1
	s_add_u32 s34, s30, 933888
	s_addc_u32 s35, s31, 0
	v_add_f32_e32 v109, v109, v62
	v_add_f32_e32 v109, v109, v173
	v_add_f32_e32 v125, v125, v63
	v_add_f32_e32 v125, v125, v189
	global_store_dword v5, v109, s[34:35] sc1
	global_store_dword v5, v125, s[34:35] offset:128 sc1
	s_add_u32 s32, s30, 950272
	s_addc_u32 s33, s31, 0
	v_add_f32_e32 v110, v110, v62
	v_add_f32_e32 v110, v110, v174
	v_add_f32_e32 v126, v126, v63
	v_add_f32_e32 v126, v126, v190
	global_store_dword v5, v110, s[32:33] sc1
	global_store_dword v5, v126, s[32:33] offset:128 sc1
	s_add_u32 s34, s30, 966656
	s_addc_u32 s35, s31, 0
	v_add_f32_e32 v111, v111, v62
	v_add_f32_e32 v111, v111, v175
	v_add_f32_e32 v127, v127, v63
	v_add_f32_e32 v127, v127, v191
	global_store_dword v5, v111, s[34:35] sc1
	global_store_dword v5, v127, s[34:35] offset:128 sc1
